# P5: per-expert global count atomic issued before the h2 section and consumed after it with a counted vmcnt(16) (round trip hidden behind the h2 arithmetic)
# baseline (speedup 1.0000x reference)
.LBB0_1115:
	s_waitcnt lgkmcnt(0)
	s_barrier
	s_and_saveexec_b64 s[0:1], s[22:23]
	ds_read_b32 v151, v253
	s_waitcnt lgkmcnt(0)
	global_atomic_add v151, v[142:143], v151, off sc0
	s_or_b64 exec, exec, s[0:1]
	v_mbcnt_lo_u32_b32 v70, -1, 0
	v_mbcnt_hi_u32_b32 v70, -1, v70
	v_readlane_b32 s18, v255, 18
	v_lshrrev_b32_e32 v70, 4, v70
	s_lshl_b32 s18, s18, 9
	v_lshlrev_b32_e32 v70, 5, v70
	s_add_i32 s18, s18, 0x12000
	v_add_u32_e32 v70, s18, v70
	ds_read_b128 v[66:69], v70 offset:16
	ds_read_b128 v[70:73], v70
	ds_read_b32 v132, v153
	v_mov_b32_e32 v78, 0
	v_mov_b32_e32 v79, 0
	s_ashr_i32 s39, s38, 31
	s_lshl_b64 s[0:1], s[38:39], 16
	s_waitcnt lgkmcnt(0)
	v_mul_f32_e32 v74, v132, v223
	v_mul_f32_e32 v75, v132, v221
	v_mul_f32_e32 v76, v132, v220
	v_mul_f32_e32 v77, v132, v219
	s_waitcnt lgkmcnt(0)
	v_mul_f32_e32 v74, v70, v74
	v_mul_f32_e32 v75, v71, v75
	v_cvt_pk_fp8_f32 v78, v74, v75
	v_mul_f32_e32 v74, v132, v214
	v_mul_f32_e32 v75, v132, v213
	v_mul_f32_e32 v74, v66, v74
	v_mul_f32_e32 v75, v67, v75
	v_cvt_pk_fp8_f32 v79, v74, v75
	v_mul_f32_e32 v76, v72, v76
	v_mul_f32_e32 v77, v73, v77
	v_cvt_pk_fp8_f32 v78, v76, v77 op_sel:[0,0,1]
	v_mul_f32_e32 v76, v132, v212
	v_mul_f32_e32 v77, v132, v211
	v_mul_f32_e32 v76, v68, v76
	v_mul_f32_e32 v77, v69, v77
	v_cvt_pk_fp8_f32 v79, v76, v77 op_sel:[0,0,1]
	v_lshl_or_b32 v74, v252, 10, s0
	v_mov_b32_e32 v75, s1
	v_lshl_add_u64 v[76:77], v[140:141], 0, v[74:75]
	global_store_dwordx2 v[76:77], v[78:79], off
	ds_read2_b32 v[78:79], v153 offset1:16
	s_waitcnt lgkmcnt(0)
	v_mul_f32_e32 v82, v79, v229
	v_mul_f32_e32 v80, v79, v230
	v_mul_f32_e32 v81, v79, v228
	v_mul_f32_e32 v83, v72, v82
	v_mul_f32_e32 v82, v79, v227
	v_mul_f32_e32 v80, v70, v80
	v_mul_f32_e32 v81, v71, v81
	v_mul_f32_e32 v84, v73, v82
	v_mov_b32_e32 v82, 0
	v_cvt_pk_fp8_f32 v82, v80, v81
	v_mul_f32_e32 v80, v79, v217
	v_mul_f32_e32 v81, v79, v218
	v_mul_f32_e32 v80, v66, v80
	v_cvt_pk_fp8_f32 v82, v83, v84 op_sel:[0,0,1]
	v_mul_f32_e32 v83, v79, v216
	v_mul_f32_e32 v84, v68, v83
	v_mul_f32_e32 v83, v79, v215
	v_mul_f32_e32 v81, v67, v81
	v_mul_f32_e32 v85, v69, v83
	v_mov_b32_e32 v83, 0
	v_cvt_pk_fp8_f32 v83, v80, v81
	v_or_b32_e32 v80, 0x4000, v74
	v_mov_b32_e32 v81, s1
	v_cvt_pk_fp8_f32 v83, v84, v85 op_sel:[0,0,1]
	v_lshl_add_u64 v[84:85], v[140:141], 0, v[80:81]
	global_store_dwordx2 v[84:85], v[82:83], off
	ds_read2_b32 v[82:83], v153 offset0:16 offset1:32
	s_waitcnt lgkmcnt(0)
	v_mul_f32_e32 v86, v83, v233
	v_mul_f32_e32 v84, v83, v234
	v_mul_f32_e32 v85, v83, v232
	v_mul_f32_e32 v87, v72, v86
	v_mul_f32_e32 v86, v83, v231
	v_mul_f32_e32 v84, v70, v84
	v_mul_f32_e32 v85, v71, v85
	v_mul_f32_e32 v130, v73, v86
	v_mov_b32_e32 v86, 0
	v_cvt_pk_fp8_f32 v86, v84, v85
	v_mul_f32_e32 v84, v83, v225
	v_mul_f32_e32 v85, v83, v226
	v_mul_f32_e32 v84, v66, v84
	v_cvt_pk_fp8_f32 v86, v87, v130 op_sel:[0,0,1]
	v_mul_f32_e32 v87, v83, v224
	v_mul_f32_e32 v130, v68, v87
	v_mul_f32_e32 v87, v83, v222
	v_mul_f32_e32 v85, v67, v85
	v_mul_f32_e32 v131, v69, v87
	v_mov_b32_e32 v87, 0
	v_cvt_pk_fp8_f32 v87, v84, v85
	v_or_b32_e32 v84, 0x8000, v74
	v_mov_b32_e32 v85, s1
	v_or_b32_e32 v74, 0xc000, v74
	v_cvt_pk_fp8_f32 v87, v130, v131 op_sel:[0,0,1]
	v_lshl_add_u64 v[130:131], v[140:141], 0, v[84:85]
	global_store_dwordx2 v[130:131], v[86:87], off
	ds_read2_b32 v[86:87], v153 offset0:32 offset1:48
	s_waitcnt lgkmcnt(0)
	v_mul_f32_e32 v130, v87, v247
	v_mul_f32_e32 v130, v70, v130
	v_mul_f32_e32 v70, v87, v245
	v_mul_f32_e32 v71, v71, v70
	v_mul_f32_e32 v70, v87, v250
	v_mul_f32_e32 v72, v72, v70
	v_mul_f32_e32 v70, v87, v249
	v_mul_f32_e32 v73, v73, v70
	v_mov_b32_e32 v70, 0
	v_cvt_pk_fp8_f32 v70, v130, v71
	v_mul_f32_e32 v71, v87, v243
	v_mul_f32_e32 v66, v66, v71
	v_mul_f32_e32 v71, v87, v248
	v_mul_f32_e32 v67, v67, v71
	v_mul_f32_e32 v71, v87, v246
	v_mul_f32_e32 v68, v68, v71
	v_mul_f32_e32 v71, v87, v244
	v_mul_f32_e32 v69, v69, v71
	v_mov_b32_e32 v71, 0
	v_cvt_pk_fp8_f32 v71, v66, v67
	v_cvt_pk_fp8_f32 v70, v72, v73 op_sel:[0,0,1]
	v_lshl_add_u64 v[66:67], v[140:141], 0, v[74:75]
	v_mul_f32_e32 v130, v132, v194
	v_cvt_pk_fp8_f32 v71, v68, v69 op_sel:[0,0,1]
	global_store_dwordx2 v[66:67], v[70:71], off
	s_nop 1
	v_mbcnt_lo_u32_b32 v70, -1, 0
	v_mbcnt_hi_u32_b32 v70, -1, v70
	v_readlane_b32 s18, v255, 18
	v_lshrrev_b32_e32 v70, 4, v70
	s_lshl_b32 s18, s18, 9
	v_lshlrev_b32_e32 v70, 5, v70
	s_add_i32 s18, s18, 0x12080
	v_add_u32_e32 v70, s18, v70
	ds_read_b128 v[66:69], v70 offset:16
	ds_read_b128 v[70:73], v70
	s_waitcnt lgkmcnt(0)
	v_mul_f32_e32 v131, v70, v130
	v_mul_f32_e32 v130, v132, v193
	v_mul_f32_e32 v133, v71, v130
	v_mul_f32_e32 v130, v132, v192
	v_mul_f32_e32 v192, v72, v130
	v_mul_f32_e32 v130, v132, v191
	v_mul_f32_e32 v191, v73, v130
	v_mov_b32_e32 v130, 0
	v_cvt_pk_fp8_f32 v130, v131, v133
	v_mul_f32_e32 v131, v132, v190
	v_mul_f32_e32 v133, v66, v131
	v_mul_f32_e32 v131, v132, v189
	v_mul_f32_e32 v189, v67, v131
	v_mul_f32_e32 v131, v132, v188
	v_mul_f32_e32 v188, v68, v131
	v_mul_f32_e32 v131, v132, v187
	v_mul_f32_e32 v132, v69, v131
	v_mov_b32_e32 v131, 0
	v_cvt_pk_fp8_f32 v131, v133, v189
	v_cvt_pk_fp8_f32 v130, v192, v191 op_sel:[0,0,1]
	v_cvt_pk_fp8_f32 v131, v188, v132 op_sel:[0,0,1]
	global_store_dwordx2 v[76:77], v[130:131], off offset:32
	v_mul_f32_e32 v130, v79, v201
	v_mul_f32_e32 v131, v70, v130
	v_mul_f32_e32 v130, v79, v202
	v_mul_f32_e32 v132, v71, v130
	v_mul_f32_e32 v130, v79, v200
	v_mul_f32_e32 v133, v72, v130
	v_mul_f32_e32 v130, v79, v199
	v_mul_f32_e32 v187, v73, v130
	v_mov_b32_e32 v130, 0
	v_cvt_pk_fp8_f32 v130, v131, v132
	v_mul_f32_e32 v131, v79, v198
	v_mul_f32_e32 v132, v66, v131
	v_mul_f32_e32 v131, v79, v197
	v_cvt_pk_fp8_f32 v130, v133, v187 op_sel:[0,0,1]
	v_mul_f32_e32 v133, v67, v131
	v_mul_f32_e32 v131, v79, v195
	v_mul_f32_e32 v187, v68, v131
	v_mov_b32_e32 v131, 0
	v_cvt_pk_fp8_f32 v131, v132, v133
	v_mul_f32_e32 v79, v79, v196
	v_mul_f32_e32 v79, v69, v79
	v_lshl_add_u64 v[132:133], v[144:145], 0, v[80:81]
	v_cvt_pk_fp8_f32 v131, v187, v79 op_sel:[0,0,1]
	v_mul_f32_e32 v79, v83, v209
	v_mul_f32_e32 v79, v70, v79
	global_store_dwordx2 v[132:133], v[130:131], off
	v_mul_f32_e32 v130, v83, v210
	v_mul_f32_e32 v131, v71, v130
	v_mul_f32_e32 v130, v83, v208
	v_mul_f32_e32 v132, v72, v130
	v_mul_f32_e32 v130, v83, v207
	v_mul_f32_e32 v133, v73, v130
	v_mov_b32_e32 v130, 0
	v_cvt_pk_fp8_f32 v130, v79, v131
	v_mul_f32_e32 v131, v83, v205
	v_mul_f32_e32 v79, v83, v206
	v_mul_f32_e32 v79, v66, v79
	v_cvt_pk_fp8_f32 v130, v132, v133 op_sel:[0,0,1]
	v_mul_f32_e32 v132, v67, v131
	v_mul_f32_e32 v131, v83, v203
	v_mul_f32_e32 v133, v68, v131
	v_mov_b32_e32 v131, 0
	v_cvt_pk_fp8_f32 v131, v79, v132
	v_mul_f32_e32 v79, v87, v236
	v_mul_f32_e32 v79, v70, v79
	v_mul_f32_e32 v70, v87, v242
	v_mul_f32_e32 v71, v71, v70
	v_mul_f32_e32 v70, v87, v240
	v_mul_f32_e32 v72, v72, v70
	v_mul_f32_e32 v70, v87, v238
	v_mul_f32_e32 v73, v73, v70
	v_mov_b32_e32 v70, 0
	v_cvt_pk_fp8_f32 v70, v79, v71
	v_mul_f32_e32 v71, v87, v239
	v_mul_f32_e32 v66, v66, v71
	v_mul_f32_e32 v71, v87, v237
	v_mul_f32_e32 v67, v67, v71
	v_mul_f32_e32 v71, v87, v235
	v_mul_f32_e32 v83, v83, v204
	v_mul_f32_e32 v68, v68, v71
	v_mul_f32_e32 v71, v87, v241
	v_mul_f32_e32 v83, v69, v83
	v_mul_f32_e32 v69, v69, v71
	v_mov_b32_e32 v71, 0
	v_cvt_pk_fp8_f32 v71, v66, v67
	v_cvt_pk_fp8_f32 v131, v133, v83 op_sel:[0,0,1]
	v_cvt_pk_fp8_f32 v70, v72, v73 op_sel:[0,0,1]
	v_lshl_add_u64 v[132:133], v[144:145], 0, v[84:85]
	v_cvt_pk_fp8_f32 v71, v68, v69 op_sel:[0,0,1]
	v_lshl_add_u64 v[66:67], v[144:145], 0, v[74:75]
	global_store_dwordx2 v[132:133], v[130:131], off
	global_store_dwordx2 v[66:67], v[70:71], off
	s_nop 1
	v_mbcnt_lo_u32_b32 v70, -1, 0
	v_mbcnt_hi_u32_b32 v70, -1, v70
	v_readlane_b32 s18, v255, 18
	v_lshrrev_b32_e32 v70, 4, v70
	s_lshl_b32 s18, s18, 9
	v_lshlrev_b32_e32 v70, 5, v70
	s_add_i32 s18, s18, 0x12100
	v_add_u32_e32 v70, s18, v70
	ds_read_b128 v[66:69], v70 offset:16
	ds_read_b128 v[70:73], v70
	ds_read_b32 v79, v153
	s_waitcnt lgkmcnt(0)
	v_mul_f32_e32 v130, v79, v178
	v_mul_f32_e32 v83, v79, v180
	v_mul_f32_e32 v87, v79, v179
	s_waitcnt lgkmcnt(0)
	v_mul_f32_e32 v131, v72, v130
	v_mul_f32_e32 v130, v79, v177
	v_mul_f32_e32 v83, v70, v83
	v_mul_f32_e32 v87, v71, v87
	v_mul_f32_e32 v132, v73, v130
	v_mov_b32_e32 v130, 0
	v_cvt_pk_fp8_f32 v130, v83, v87
	v_mul_f32_e32 v83, v79, v176
	v_mul_f32_e32 v87, v79, v175
	v_mul_f32_e32 v83, v66, v83
	v_cvt_pk_fp8_f32 v130, v131, v132 op_sel:[0,0,1]
	v_mul_f32_e32 v131, v79, v174
	v_mul_f32_e32 v87, v67, v87
	v_mul_f32_e32 v132, v68, v131
	v_mov_b32_e32 v131, 0
	v_cvt_pk_fp8_f32 v131, v83, v87
	v_mul_f32_e32 v79, v79, v173
	v_mul_f32_e32 v79, v69, v79
	v_cvt_pk_fp8_f32 v131, v132, v79 op_sel:[0,0,1]
	ds_read_b32 v79, v153 offset:64
	global_store_dwordx2 v[76:77], v[130:131], off offset:64
	s_waitcnt lgkmcnt(0)
	v_mul_f32_e32 v130, v79, v183
	v_mul_f32_e32 v83, v79, v184
	v_mul_f32_e32 v87, v79, v182
	v_mul_f32_e32 v131, v72, v130
	v_mul_f32_e32 v130, v79, v181
	v_mul_f32_e32 v83, v70, v83
	v_mul_f32_e32 v87, v71, v87
	v_mul_f32_e32 v132, v73, v130
	v_mov_b32_e32 v130, 0
	v_cvt_pk_fp8_f32 v130, v83, v87
	v_mul_f32_e32 v83, v79, v128
	v_mul_f32_e32 v87, v79, v129
	v_mul_f32_e32 v83, v66, v83
	v_cvt_pk_fp8_f32 v130, v131, v132 op_sel:[0,0,1]
	v_mul_f32_e32 v87, v67, v87
	v_mov_b32_e32 v131, 0
	v_cvt_pk_fp8_f32 v131, v83, v87
	v_mul_f32_e32 v127, v79, v127
	v_mul_f32_e32 v79, v79, v126
	v_mul_f32_e32 v127, v68, v127
	v_mul_f32_e32 v79, v69, v79
	v_cvt_pk_fp8_f32 v131, v127, v79 op_sel:[0,0,1]
	ds_read_b32 v79, v153 offset:128
	v_lshl_add_u64 v[126:127], v[146:147], 0, v[80:81]
	global_store_dwordx2 v[126:127], v[130:131], off
	s_waitcnt lgkmcnt(0)
	v_mul_f32_e32 v83, v79, v117
	v_mul_f32_e32 v87, v79, v115
	v_mul_f32_e32 v114, v79, v114
	v_mul_f32_e32 v83, v70, v83
	v_mul_f32_e32 v87, v71, v87
	v_mul_f32_e32 v115, v79, v116
	v_mul_f32_e32 v116, v73, v114
	v_mov_b32_e32 v114, 0
	v_cvt_pk_fp8_f32 v114, v83, v87
	v_mul_f32_e32 v115, v72, v115
	v_mul_f32_e32 v83, v79, v112
	v_mul_f32_e32 v87, v79, v113
	v_cvt_pk_fp8_f32 v114, v115, v116 op_sel:[0,0,1]
	v_mul_f32_e32 v83, v66, v83
	v_mul_f32_e32 v87, v67, v87
	v_mov_b32_e32 v115, 0
	v_cvt_pk_fp8_f32 v115, v83, v87
	v_mul_f32_e32 v111, v79, v111
	v_mul_f32_e32 v79, v79, v110
	v_mul_f32_e32 v111, v68, v111
	v_mul_f32_e32 v79, v69, v79
	v_cvt_pk_fp8_f32 v115, v111, v79 op_sel:[0,0,1]
	ds_read_b32 v79, v153 offset:192
	v_lshl_add_u64 v[110:111], v[146:147], 0, v[84:85]
	v_mul_f32_e32 v87, v78, v171
	global_store_dwordx2 v[110:111], v[114:115], off
	s_waitcnt lgkmcnt(0)
	v_mul_f32_e32 v83, v79, v100
	v_mul_f32_e32 v83, v70, v83
	v_mul_f32_e32 v70, v79, v98
	v_mul_f32_e32 v71, v71, v70
	v_mul_f32_e32 v70, v79, v186
	v_mul_f32_e32 v72, v72, v70
	v_mul_f32_e32 v70, v79, v185
	v_mul_f32_e32 v73, v73, v70
	v_mov_b32_e32 v70, 0
	v_cvt_pk_fp8_f32 v70, v83, v71
	v_mul_f32_e32 v71, v79, v96
	v_mul_f32_e32 v66, v66, v71
	v_mul_f32_e32 v71, v79, v101
	v_mul_f32_e32 v67, v67, v71
	v_mul_f32_e32 v71, v79, v99
	v_mul_f32_e32 v68, v68, v71
	v_mul_f32_e32 v71, v79, v97
	v_mul_f32_e32 v69, v69, v71
	v_mov_b32_e32 v71, 0
	v_cvt_pk_fp8_f32 v71, v66, v67
	v_cvt_pk_fp8_f32 v70, v72, v73 op_sel:[0,0,1]
	v_lshl_add_u64 v[66:67], v[146:147], 0, v[74:75]
	v_mul_f32_e32 v79, v78, v165
	v_cvt_pk_fp8_f32 v71, v68, v69 op_sel:[0,0,1]
	v_mul_f32_e32 v83, v78, v172
	v_mul_f32_e32 v96, v78, v170
	global_store_dwordx2 v[66:67], v[70:71], off
	s_nop 1
	v_mbcnt_lo_u32_b32 v70, -1, 0
	v_mbcnt_hi_u32_b32 v70, -1, v70
	v_readlane_b32 s18, v255, 18
	v_lshrrev_b32_e32 v70, 4, v70
	s_lshl_b32 s18, s18, 9
	v_lshlrev_b32_e32 v70, 5, v70
	s_add_i32 s18, s18, 0x12180
	v_add_u32_e32 v70, s18, v70
	ds_read_b128 v[66:69], v70 offset:16
	ds_read_b128 v[70:73], v70
	s_waitcnt lgkmcnt(0)
	v_mul_f32_e32 v79, v70, v79
	v_mul_f32_e32 v83, v71, v83
	v_mul_f32_e32 v97, v73, v96
	v_mov_b32_e32 v96, 0
	v_cvt_pk_fp8_f32 v96, v79, v83
	v_mul_f32_e32 v87, v72, v87
	v_mul_f32_e32 v79, v78, v169
	v_mul_f32_e32 v83, v78, v168
	v_cvt_pk_fp8_f32 v96, v87, v97 op_sel:[0,0,1]
	v_mul_f32_e32 v79, v66, v79
	v_mul_f32_e32 v83, v67, v83
	v_mov_b32_e32 v97, 0
	v_cvt_pk_fp8_f32 v97, v79, v83
	v_mul_f32_e32 v87, v78, v167
	v_mul_f32_e32 v78, v78, v166
	v_mul_f32_e32 v87, v68, v87
	v_mul_f32_e32 v78, v69, v78
	v_cvt_pk_fp8_f32 v97, v87, v78 op_sel:[0,0,1]
	global_store_dwordx2 v[76:77], v[96:97], off offset:96
	v_mul_f32_e32 v76, v82, v125
	v_mul_f32_e32 v77, v70, v76
	v_mul_f32_e32 v76, v82, v124
	v_mul_f32_e32 v78, v71, v76
	v_mul_f32_e32 v76, v82, v123
	v_mul_f32_e32 v79, v72, v76
	v_mul_f32_e32 v76, v82, v122
	v_mul_f32_e32 v83, v73, v76
	v_mov_b32_e32 v76, 0
	v_cvt_pk_fp8_f32 v76, v77, v78
	v_mul_f32_e32 v77, v82, v121
	v_mul_f32_e32 v78, v66, v77
	v_mul_f32_e32 v77, v82, v120
	v_cvt_pk_fp8_f32 v76, v79, v83 op_sel:[0,0,1]
	v_mul_f32_e32 v79, v67, v77
	v_mul_f32_e32 v77, v82, v119
	v_mul_f32_e32 v83, v68, v77
	v_mul_f32_e32 v77, v82, v118
	v_mul_f32_e32 v82, v69, v77
	v_mov_b32_e32 v77, 0
	v_cvt_pk_fp8_f32 v77, v78, v79
	v_lshl_add_u64 v[78:79], v[148:149], 0, v[80:81]
	v_cvt_pk_fp8_f32 v77, v83, v82 op_sel:[0,0,1]
	global_store_dwordx2 v[78:79], v[76:77], off
	v_mul_f32_e32 v76, v86, v109
	v_mul_f32_e32 v77, v70, v76
	v_mul_f32_e32 v76, v86, v108
	v_mul_f32_e32 v78, v71, v76
	v_mul_f32_e32 v76, v86, v107
	v_mul_f32_e32 v79, v72, v76
	v_mul_f32_e32 v76, v86, v106
	v_mul_f32_e32 v80, v73, v76
	v_mov_b32_e32 v76, 0
	v_cvt_pk_fp8_f32 v76, v77, v78
	v_mul_f32_e32 v77, v86, v105
	v_mul_f32_e32 v78, v66, v77
	v_mul_f32_e32 v77, v86, v104
	v_cvt_pk_fp8_f32 v76, v79, v80 op_sel:[0,0,1]
	v_mul_f32_e32 v79, v67, v77
	v_mul_f32_e32 v77, v86, v103
	v_mul_f32_e32 v80, v68, v77
	v_mul_f32_e32 v77, v86, v102
	v_mul_f32_e32 v81, v69, v77
	v_mov_b32_e32 v77, 0
	v_cvt_pk_fp8_f32 v77, v78, v79
	v_lshl_add_u64 v[78:79], v[148:149], 0, v[84:85]
	v_cvt_pk_fp8_f32 v77, v80, v81 op_sel:[0,0,1]
	global_store_dwordx2 v[78:79], v[76:77], off
	ds_read_b32 v76, v153 offset:192
	s_waitcnt lgkmcnt(0)
	v_mul_f32_e32 v77, v76, v95
	v_mul_f32_e32 v77, v70, v77
	v_mul_f32_e32 v70, v76, v94
	v_mul_f32_e32 v71, v71, v70
	v_mul_f32_e32 v70, v76, v93
	v_mul_f32_e32 v72, v72, v70
	v_mul_f32_e32 v70, v76, v92
	v_mul_f32_e32 v73, v73, v70
	v_mov_b32_e32 v70, 0
	v_cvt_pk_fp8_f32 v70, v77, v71
	v_mul_f32_e32 v71, v76, v91
	v_mul_f32_e32 v66, v66, v71
	v_mul_f32_e32 v71, v76, v90
	v_mul_f32_e32 v67, v67, v71
	v_mul_f32_e32 v71, v76, v89
	v_mul_f32_e32 v68, v68, v71
	v_mul_f32_e32 v71, v76, v88
	v_mul_f32_e32 v69, v69, v71
	v_mov_b32_e32 v71, 0
	v_cvt_pk_fp8_f32 v71, v66, v67
	v_cvt_pk_fp8_f32 v70, v72, v73 op_sel:[0,0,1]
	v_lshl_add_u64 v[66:67], v[148:149], 0, v[74:75]
	v_cvt_pk_fp8_f32 v71, v68, v69 op_sel:[0,0,1]
	global_store_dwordx2 v[66:67], v[70:71], off
	s_and_saveexec_b64 s[0:1], s[22:23]
	s_cbranch_execz .LBB0_1117
	s_waitcnt vmcnt(16)
	ds_write_b32 v254, v151
.LBB0_1117:
	s_or_b64 exec, exec, s[0:1]
	s_waitcnt lgkmcnt(0)
	v_lshlrev_b32_e32 v151, 2, v0
	v_add_u32_e32 v151, 0x10800, v151
	s_barrier
	s_and_saveexec_b64 s[0:1], s[16:17]
	s_cbranch_execz .LBB0_1034
	ds_read_b32 v66, v154
	ds_read_b32 v70, v155
	v_lshrrev_b32_e32 v67, 2, v0
	v_or_b32_e32 v72, s35, v67
	v_lshl_or_b32 v68, s38, 8, v0
	s_waitcnt lgkmcnt(1)
	v_lshl_add_u32 v67, v66, 2, 0
	v_add_u32_e32 v67, 0x205a0, v67
	ds_read_b32 v71, v67
	v_ashrrev_i32_e32 v67, 31, v66
	v_lshlrev_b64 v[66:67], 16, v[66:67]
	v_ashrrev_i32_e32 v69, 31, v68
	v_lshl_add_u64 v[66:67], s[52:53], 0, v[66:67]
	s_waitcnt lgkmcnt(0)
	v_add_u32_e32 v70, v70, v71
	v_ashrrev_i32_e32 v71, 31, v70
	v_lshl_add_u64 v[68:69], v[68:69], 2, s[44:45]
	v_lshl_add_u64 v[66:67], v[70:71], 2, v[66:67]
	global_store_dword v[68:69], v70, off
	global_store_dword v[66:67], v72, off
	s_branch .LBB0_1034
